# indexer step 1: query fragments of heads 0-7 preloaded once per unit into 128 otherwise idle VGPRs (32 fewer ds_read_b128 and 29 fewer waits per key tile; MFMA->VALU pads restored to 12 states)
# speedup vs baseline: 1.0043x; 1.0043x over previous
.LBB0_378:
	v_cndmask_b32_e64 v2, 0, 1, s[16:17]
	v_cmp_ne_u32_e64 s[22:23], 1, v2
	s_andn2_b64 vcc, exec, s[16:17]
	s_cbranch_vccnz .LBB0_391
	s_waitcnt vmcnt(0)
	v_lshlrev_b32_e32 v2, 16, v4
	v_and_b32_e32 v4, 0xffff0000, v4
	v_mul_f32_e32 v249, 0x3cb504f3, v4
	v_lshlrev_b32_e32 v4, 16, v5
	v_mul_f32_e32 v250, 0x3cb504f3, v4
	v_and_b32_e32 v4, 0xffff0000, v5
	v_lshlrev_b32_e32 v5, 2, v10
	v_mul_f32_e32 v251, 0x3cb504f3, v4
	v_lshlrev_b32_e32 v4, 16, v6
	v_add_u32_e32 v10, s89, v5
	v_mul_f32_e32 v252, 0x3cb504f3, v4
	v_and_b32_e32 v4, 0xffff0000, v6
	v_or_b32_e32 v6, s89, v8
	v_cmp_gt_i32_e64 s[24:25], v5, v8
	v_cmp_lt_i32_e64 s[26:27], v5, v8
	v_or_b32_e32 v5, 2, v10
	v_cmp_gt_i32_e64 s[28:29], v5, v6
	v_or_b32_e32 v5, 3, v10
	v_cmp_gt_i32_e64 s[30:31], v5, v6
	v_add_u32_e32 v5, 8, v10
	v_cmp_gt_i32_e64 s[34:35], v5, v6
	v_add_u32_e32 v5, 9, v10
	v_cmp_gt_i32_e64 s[36:37], v5, v6
	v_add_u32_e32 v5, 10, v10
	v_cmp_gt_i32_e64 s[38:39], v5, v6
	v_add_u32_e32 v5, 11, v10
	v_cmp_gt_i32_e64 s[40:41], v5, v6
	v_add_u32_e32 v5, 16, v10
	v_cmp_gt_i32_e64 s[42:43], v5, v6
	v_add_u32_e32 v5, 17, v10
	s_mov_b64 s[68:69], s[20:21]
	s_mov_b64 s[20:21], s[44:45]
	v_cmp_gt_i32_e64 s[44:45], v5, v6
	v_add_u32_e32 v5, 18, v10
	s_mov_b64 s[74:75], s[46:47]
	v_cmp_gt_i32_e64 s[46:47], v5, v6
	v_add_u32_e32 v5, 19, v10
	s_mov_b64 s[14:15], s[48:49]
	v_cmp_gt_i32_e64 s[48:49], v5, v6
	v_add_u32_e32 v5, 24, v10
	s_mov_b32 s78, s6
	s_mov_b32 s6, s4
	s_mov_b32 s4, s3
	s_mov_b32 s71, s2
	s_mov_b64 s[2:3], s[64:65]
	s_mov_b32 s64, s62
	s_mov_b64 s[62:63], s[50:51]
	v_mul_f32_e32 v253, 0x3cb504f3, v4
	v_lshlrev_b32_e32 v4, 16, v7
	v_cmp_gt_i32_e64 s[50:51], v5, v6
	v_add_u32_e32 v5, 25, v10
	v_writelane_b32 v255, s60, 30
	s_mov_b64 s[84:85], s[10:11]
	s_mov_b64 s[10:11], s[8:9]
	s_mov_b64 s[8:9], s[52:53]
	v_mul_f32_e32 v223, 0x3cb504f3, v4
	v_and_b32_e32 v4, 0xffff0000, v7
	s_movk_i32 s0, 0x410
	v_cmp_gt_i32_e64 s[52:53], v5, v6
	v_add_u32_e32 v5, 26, v10
	s_mov_b32 s80, s54
	v_mul_f32_e32 v219, 0x3cb504f3, v4
	v_lshlrev_b32_e32 v4, 4, v9
	v_mad_u32_u24 v222, v8, s0, 0
	v_lshlrev_b32_e32 v7, 6, v8
	v_and_b32_e32 v9, 0xffffffe0, v9
	v_cmp_gt_i32_e64 s[54:55], v5, v6
	v_add_u32_e32 v5, 27, v10
	v_readlane_b32 s0, v255, 7
	s_mov_b32 s73, s57
	v_mul_f32_e32 v2, 0x3cb504f3, v2
	v_cmp_gt_i32_e64 s[56:57], v5, v6
	v_add3_u32 v231, s0, v7, v9
	v_add_u32_e32 v214, 0, v4
	v_readlane_b32 s95, v255, 6
	s_mov_b32 s0, s58
	s_mov_b32 s65, 0x5040100
	ds_read_b128 v[84:87], v214
	ds_read_b128 v[88:91], v214 offset:1024
	ds_read_b128 v[92:95], v214 offset:2048
	ds_read_b128 v[96:99], v214 offset:3072
	ds_read_b128 v[100:103], v214 offset:4096
	ds_read_b128 v[104:107], v214 offset:5120
	ds_read_b128 v[108:111], v214 offset:6144
	ds_read_b128 v[112:115], v214 offset:7168
	ds_read_b128 v[116:119], v214 offset:8192
	ds_read_b128 v[120:123], v214 offset:9216
	ds_read_b128 v[124:127], v214 offset:10240
	ds_read_b128 v[128:131], v214 offset:11264
	ds_read_b128 v[132:135], v214 offset:12288
	ds_read_b128 v[136:139], v214 offset:13312
	ds_read_b128 v[140:143], v214 offset:14336
	ds_read_b128 v[144:147], v214 offset:15360
	ds_read_b128 v[148:151], v214 offset:16384
	ds_read_b128 v[152:155], v214 offset:17408
	ds_read_b128 v[156:159], v214 offset:18432
	ds_read_b128 v[160:163], v214 offset:19456
	ds_read_b128 v[164:167], v214 offset:20480
	ds_read_b128 v[168:171], v214 offset:21504
	ds_read_b128 v[172:175], v214 offset:22528
	ds_read_b128 v[176:179], v214 offset:23552
	ds_read_b128 v[180:183], v214 offset:24576
	ds_read_b128 v[184:187], v214 offset:25600
	ds_read_b128 v[188:191], v214 offset:26624
	ds_read_b128 v[192:195], v214 offset:27648
	ds_read_b128 v[196:199], v214 offset:28672
	ds_read_b128 v[200:203], v214 offset:29696
	ds_read_b128 v[204:207], v214 offset:30720
	ds_read_b128 v[208:211], v214 offset:31744
	s_waitcnt lgkmcnt(0)

.LBB0_382:
	s_cmp_eq_u32 s81, s0
	s_mov_b64 s[0:1], -1
	v_mfma_f32_32x32x16_bf16 v[10:25], v[80:83], v[84:87], 0
	v_mfma_f32_32x32x16_bf16 v[10:25], v[76:79], v[88:91], v[10:25]
	v_mfma_f32_32x32x16_bf16 v[10:25], v[72:75], v[92:95], v[10:25]
	v_mfma_f32_32x32x16_bf16 v[10:25], v[52:55], v[96:99], v[10:25]
	s_nop 11
	v_fma_f32 v48, |v10|, v2, 0
	v_fma_f32 v49, |v11|, v2, 0
	v_fma_f32 v50, |v12|, v2, 0
	v_fma_f32 v51, |v13|, v2, 0
	v_fma_f32 v212, |v14|, v2, 0
	v_fma_f32 v213, |v15|, v2, 0
	v_fma_f32 v215, |v16|, v2, 0
	v_fma_f32 v216, |v17|, v2, 0
	v_fma_f32 v217, |v18|, v2, 0
	v_fma_f32 v228, |v19|, v2, 0
	v_mfma_f32_32x32x16_bf16 v[4:19], v[80:83], v[100:103], 0
	v_fma_f32 v229, |v20|, v2, 0
	v_fma_f32 v230, |v21|, v2, 0
	v_mfma_f32_32x32x16_bf16 v[4:19], v[76:79], v[104:107], v[4:19]
	v_fma_f32 v234, |v22|, v2, 0
	v_fma_f32 v235, |v23|, v2, 0
	v_mfma_f32_32x32x16_bf16 v[4:19], v[72:75], v[108:111], v[4:19]
	v_fma_f32 v236, |v24|, v2, 0
	v_fma_f32 v237, |v25|, v2, 0
	v_mfma_f32_32x32x16_bf16 v[4:19], v[52:55], v[112:115], v[4:19]
	s_nop 11
	v_fma_f32 v48, |v4|, v249, v48
	v_mfma_f32_32x32x16_bf16 v[20:35], v[80:83], v[116:119], 0
	v_fma_f32 v49, |v5|, v249, v49
	v_fma_f32 v50, |v6|, v249, v50
	v_fma_f32 v51, |v7|, v249, v51
	v_mfma_f32_32x32x16_bf16 v[20:35], v[76:79], v[120:123], v[20:35]
	v_fma_f32 v8, |v8|, v249, v212
	v_fma_f32 v9, |v9|, v249, v213
	v_fma_f32 v10, |v10|, v249, v215
	v_fma_f32 v11, |v11|, v249, v216
	v_mfma_f32_32x32x16_bf16 v[20:35], v[72:75], v[124:127], v[20:35]
	v_fma_f32 v12, |v12|, v249, v217
	v_fma_f32 v13, |v13|, v249, v228
	v_fma_f32 v212, |v14|, v249, v229
	v_fma_f32 v213, |v15|, v249, v230
	v_fma_f32 v215, |v16|, v249, v234
	v_fma_f32 v216, |v17|, v249, v235
	v_fma_f32 v217, |v18|, v249, v236
	v_fma_f32 v228, |v19|, v249, v237
	v_mfma_f32_32x32x16_bf16 v[20:35], v[52:55], v[128:131], v[20:35]
	s_nop 11
	v_fma_f32 v24, |v24|, v250, v8
	v_fma_f32 v25, |v25|, v250, v9
	v_fma_f32 v26, |v26|, v250, v10
	v_fma_f32 v27, |v27|, v250, v11
	v_fma_f32 v28, |v28|, v250, v12
	v_fma_f32 v29, |v29|, v250, v13
	v_mfma_f32_32x32x16_bf16 v[4:19], v[80:83], v[132:135], 0
	v_fma_f32 v48, |v20|, v250, v48
	v_fma_f32 v49, |v21|, v250, v49
	v_fma_f32 v50, |v22|, v250, v50
	v_fma_f32 v51, |v23|, v250, v51
	v_mfma_f32_32x32x16_bf16 v[4:19], v[76:79], v[136:139], v[4:19]
	v_fma_f32 v212, |v30|, v250, v212
	v_mfma_f32_32x32x16_bf16 v[4:19], v[72:75], v[140:143], v[4:19]
	v_fma_f32 v213, |v31|, v250, v213
	v_fma_f32 v215, |v32|, v250, v215
	v_fma_f32 v216, |v33|, v250, v216
	v_fma_f32 v217, |v34|, v250, v217
	v_fma_f32 v228, |v35|, v250, v228
	v_mfma_f32_32x32x16_bf16 v[4:19], v[52:55], v[144:147], v[4:19]
	s_nop 11
	v_fma_f32 v229, |v8|, v251, v24
	v_fma_f32 v230, |v9|, v251, v25
	v_fma_f32 v234, |v10|, v251, v26
	v_fma_f32 v235, |v11|, v251, v27
	v_fma_f32 v236, |v12|, v251, v28
	v_fma_f32 v237, |v13|, v251, v29
	v_mfma_f32_32x32x16_bf16 v[20:35], v[80:83], v[148:151], 0
	v_fma_f32 v48, |v4|, v251, v48
	v_fma_f32 v49, |v5|, v251, v49
	v_fma_f32 v50, |v6|, v251, v50
	v_fma_f32 v51, |v7|, v251, v51
	v_mfma_f32_32x32x16_bf16 v[20:35], v[76:79], v[152:155], v[20:35]
	v_fma_f32 v212, |v14|, v251, v212
	v_mfma_f32_32x32x16_bf16 v[20:35], v[72:75], v[156:159], v[20:35]
	v_fma_f32 v213, |v15|, v251, v213
	v_fma_f32 v215, |v16|, v251, v215
	v_fma_f32 v216, |v17|, v251, v216
	v_fma_f32 v217, |v18|, v251, v217
	v_fma_f32 v228, |v19|, v251, v228
	v_mfma_f32_32x32x16_bf16 v[20:35], v[52:55], v[160:163], v[20:35]
	s_nop 11
	v_fma_f32 v20, |v20|, v252, v48
	v_fma_f32 v21, |v21|, v252, v49
	v_fma_f32 v22, |v22|, v252, v50
	v_fma_f32 v23, |v23|, v252, v51
	v_mfma_f32_32x32x16_bf16 v[36:51], v[80:83], v[164:167], 0
	v_fma_f32 v24, |v24|, v252, v229
	v_fma_f32 v25, |v25|, v252, v230
	v_mfma_f32_32x32x16_bf16 v[36:51], v[76:79], v[168:171], v[36:51]
	v_fma_f32 v26, |v26|, v252, v234
	v_fma_f32 v27, |v27|, v252, v235
	v_mfma_f32_32x32x16_bf16 v[36:51], v[72:75], v[172:175], v[36:51]
	v_fma_f32 v229, |v28|, v252, v236
	v_fma_f32 v230, |v29|, v252, v237
	v_fma_f32 v212, |v30|, v252, v212
	v_fma_f32 v213, |v31|, v252, v213
	v_fma_f32 v215, |v32|, v252, v215
	v_fma_f32 v216, |v33|, v252, v216
	v_fma_f32 v217, |v34|, v252, v217
	v_fma_f32 v228, |v35|, v252, v228
	v_mfma_f32_32x32x16_bf16 v[36:51], v[52:55], v[176:179], v[36:51]
	s_nop 11
	v_fma_f32 v234, |v36|, v253, v20
	v_fma_f32 v235, |v37|, v253, v21
	v_fma_f32 v236, |v38|, v253, v22
	v_fma_f32 v237, |v39|, v253, v23
	v_fma_f32 v40, |v40|, v253, v24
	v_fma_f32 v41, |v41|, v253, v25
	v_fma_f32 v42, |v42|, v253, v26
	v_fma_f32 v43, |v43|, v253, v27
	v_mfma_f32_32x32x16_bf16 v[12:27], v[80:83], v[180:183], 0
	v_fma_f32 v44, |v44|, v253, v229
	v_fma_f32 v45, |v45|, v253, v230
	v_mfma_f32_32x32x16_bf16 v[12:27], v[76:79], v[184:187], v[12:27]
	v_fma_f32 v46, |v46|, v253, v212
	v_fma_f32 v47, |v47|, v253, v213
	v_mfma_f32_32x32x16_bf16 v[12:27], v[72:75], v[188:191], v[12:27]
	v_fma_f32 v48, |v48|, v253, v215
	v_fma_f32 v49, |v49|, v253, v216
	v_fma_f32 v50, |v50|, v253, v217
	v_fma_f32 v51, |v51|, v253, v228
	v_mfma_f32_32x32x16_bf16 v[12:27], v[52:55], v[192:195], v[12:27]
	s_nop 11
	v_fma_f32 v212, |v12|, v223, v234
	v_fma_f32 v213, |v13|, v223, v235
	v_fma_f32 v215, |v14|, v223, v236
	v_fma_f32 v216, |v15|, v223, v237
	v_fma_f32 v217, |v16|, v223, v40
	v_fma_f32 v228, |v17|, v223, v41
	v_fma_f32 v229, |v18|, v223, v42
	v_fma_f32 v230, |v19|, v223, v43
	v_mfma_f32_32x32x16_bf16 v[4:19], v[80:83], v[196:199], 0
	v_fma_f32 v234, |v20|, v223, v44
	v_fma_f32 v235, |v21|, v223, v45
	v_mfma_f32_32x32x16_bf16 v[4:19], v[76:79], v[200:203], v[4:19]
	v_fma_f32 v236, |v22|, v223, v46
	v_fma_f32 v237, |v23|, v223, v47
	v_mfma_f32_32x32x16_bf16 v[4:19], v[72:75], v[204:207], v[4:19]
	v_fma_f32 v48, |v24|, v223, v48
	v_fma_f32 v49, |v25|, v223, v49
	v_fma_f32 v50, |v26|, v223, v50
	v_fma_f32 v51, |v27|, v223, v51
	v_mfma_f32_32x32x16_bf16 v[4:19], v[52:55], v[208:211], v[4:19]
	ds_read_b128 v[20:23], v214 offset:32768
	ds_read_b128 v[36:39], v214 offset:33792
	ds_read_b128 v[40:43], v214 offset:34816
	ds_read_b128 v[44:47], v214 offset:35840
	s_waitcnt lgkmcnt(3)
	v_mfma_f32_32x32x16_bf16 v[20:35], v[80:83], v[20:23], 0
	s_nop 5
	v_fma_f32 v212, |v4|, v219, v212
	v_fma_f32 v213, |v5|, v219, v213
	v_fma_f32 v4, |v6|, v219, v215
	v_fma_f32 v5, |v7|, v219, v216
	s_waitcnt lgkmcnt(2)
	v_mfma_f32_32x32x16_bf16 v[20:35], v[76:79], v[36:39], v[20:35]
	v_fma_f32 v6, |v8|, v219, v217
	v_fma_f32 v7, |v9|, v219, v228
	v_fma_f32 v8, |v10|, v219, v229
	v_fma_f32 v9, |v11|, v219, v230
	s_waitcnt lgkmcnt(1)
	v_mfma_f32_32x32x16_bf16 v[20:35], v[72:75], v[40:43], v[20:35]
	v_fma_f32 v36, |v12|, v219, v234
	v_fma_f32 v37, |v13|, v219, v235
	v_fma_f32 v38, |v14|, v219, v236
	v_fma_f32 v39, |v15|, v219, v237
	s_waitcnt lgkmcnt(0)
	v_mfma_f32_32x32x16_bf16 v[20:35], v[52:55], v[44:47], v[20:35]
	v_fma_f32 v16, |v16|, v219, v48
	v_fma_f32 v17, |v17|, v219, v49
	s_nop 9
	v_add_f32_e32 v20, v212, v20
	v_pk_add_f32 v[14:15], v[4:5], v[22:23]
	v_pk_add_f32 v[4:5], v[32:33], v[16:17]
	v_cvt_f16_f32_e32 v16, v20
	v_fma_f32 v18, |v18|, v219, v50
	v_fma_f32 v19, |v19|, v219, v51
	v_add_f32_e32 v21, v213, v21
	v_add_f32_e32 v17, v34, v18
	v_add_f32_e32 v19, v35, v19
	v_bitop3_b32 v18, v16, s7, v16 bitop3:0xc
	v_or_b32_e32 v20, 0x8000, v16
	v_cmp_gt_i16_e32 vcc, 0, v16
	v_pk_add_f32 v[10:11], v[8:9], v[26:27]
	v_pk_add_f32 v[8:9], v[36:37], v[28:29]
	v_cndmask_b32_e32 v26, v20, v18, vcc
	v_cvt_f16_f32_e32 v29, v21
	v_cvt_f16_f32_e32 v18, v17
	v_cvt_f16_f32_e32 v17, v19
	v_pk_add_f32 v[12:13], v[6:7], v[24:25]
	v_pk_add_f32 v[6:7], v[38:39], v[30:31]
	v_bitop3_b32 v30, v29, s7, v29 bitop3:0xc
	v_or_b32_e32 v31, 0x8000, v29
	v_cmp_gt_i16_e64 s[60:61], 0, v29
	v_bitop3_b32 v21, v18, s7, v18 bitop3:0xc
	v_or_b32_e32 v22, 0x8000, v18
	v_cmp_gt_i16_e64 s[58:59], 0, v18
	v_bitop3_b32 v19, v17, s7, v17 bitop3:0xc
	v_or_b32_e32 v20, 0x8000, v17
	v_cmp_gt_i16_e32 vcc, 0, v17
	s_cbranch_scc1 .LBB0_384
	v_bfe_u32 v16, v26, 8, 8
	v_lshl_add_u32 v16, v16, 2, v222
	ds_add_u32 v16, v224 offset:36864
	v_cndmask_b32_e64 v16, v31, v30, s[60:61]
	v_cndmask_b32_e32 v40, v20, v19, vcc
	v_cndmask_b32_e64 v38, v22, v21, s[58:59]
	v_bfe_u32 v23, v16, 8, 8
	v_lshl_add_u32 v23, v23, 2, v222
	ds_add_u32 v23, v224 offset:36864
	v_lshrrev_b32_e32 v41, 8, v40
	v_bfe_u32 v24, v38, 8, 8
	v_lshl_add_u32 v24, v24, 2, v222
	ds_add_u32 v24, v224 offset:36864
	s_mov_b64 s[0:1], 0
	v_cvt_pk_f16_f32 v23, v6, v7
	v_pk_ashrrev_i16 v24, 15, v23 op_sel_hi:[0,1]
	v_bitop3_b32 v7, v23, v24, s32 bitop3:0x1e
	v_pk_lshrrev_b16 v23, 8, v7 op_sel_hi:[0,1]
	v_and_b32_e32 v24, 0xff, v23
	v_lshl_add_u32 v24, v24, 2, v222
	v_lshrrev_b32_e32 v23, 14, v23
	ds_add_u32 v24, v224 offset:36864
	v_add_u32_e32 v23, v222, v23
	ds_add_u32 v23, v224 offset:36864
	v_cvt_pk_f16_f32 v25, v8, v9
	v_pk_ashrrev_i16 v27, 15, v25 op_sel_hi:[0,1]
	v_bitop3_b32 v6, v25, v27, s32 bitop3:0x1e
	v_pk_lshrrev_b16 v25, 8, v6 op_sel_hi:[0,1]
	v_and_b32_e32 v27, 0xff, v25
	v_lshl_add_u32 v27, v27, 2, v222
	v_lshrrev_b32_e32 v25, 14, v25
	ds_add_u32 v27, v224 offset:36864
	v_add_u32_e32 v25, v222, v25
	ds_add_u32 v25, v224 offset:36864
	v_cvt_pk_f16_f32 v28, v10, v11
	v_pk_ashrrev_i16 v32, 15, v28 op_sel_hi:[0,1]
	v_bitop3_b32 v9, v28, v32, s32 bitop3:0x1e
	v_pk_lshrrev_b16 v28, 8, v9 op_sel_hi:[0,1]
	v_and_b32_e32 v32, 0xff, v28
	v_lshl_add_u32 v32, v32, 2, v222
	v_lshrrev_b32_e32 v28, 14, v28
	ds_add_u32 v32, v224 offset:36864
	v_add_u32_e32 v28, v222, v28
	ds_add_u32 v28, v224 offset:36864
	v_cvt_pk_f16_f32 v33, v12, v13
	v_pk_ashrrev_i16 v34, 15, v33 op_sel_hi:[0,1]
	v_bitop3_b32 v8, v33, v34, s32 bitop3:0x1e
	v_pk_lshrrev_b16 v33, 8, v8 op_sel_hi:[0,1]
	v_and_b32_e32 v34, 0xff, v33
	v_lshl_add_u32 v34, v34, 2, v222
	v_lshrrev_b32_e32 v33, 14, v33
	ds_add_u32 v34, v224 offset:36864
	v_add_u32_e32 v33, v222, v33
	ds_add_u32 v33, v224 offset:36864
	v_cvt_pk_f16_f32 v35, v4, v5
	v_pk_ashrrev_i16 v36, 15, v35 op_sel_hi:[0,1]
	v_bitop3_b32 v10, v35, v36, s32 bitop3:0x1e
	v_pk_lshrrev_b16 v35, 8, v10 op_sel_hi:[0,1]
	v_and_b32_e32 v36, 0xff, v35
	v_lshl_add_u32 v36, v36, 2, v222
	v_lshrrev_b32_e32 v35, 14, v35
	ds_add_u32 v36, v224 offset:36864
	v_add_u32_e32 v35, v222, v35
	ds_add_u32 v35, v224 offset:36864
	v_cvt_pk_f16_f32 v37, v14, v15
	v_pk_ashrrev_i16 v39, 15, v37 op_sel_hi:[0,1]
	v_bitop3_b32 v5, v37, v39, s32 bitop3:0x1e
	v_pk_lshrrev_b16 v37, 8, v5 op_sel_hi:[0,1]
	v_and_b32_e32 v39, 0xff, v37
	v_lshl_add_u32 v39, v39, 2, v222
	v_lshrrev_b32_e32 v37, 14, v37
	ds_add_u32 v39, v224 offset:36864
	v_add_u32_e32 v37, v222, v37
	ds_add_u32 v37, v224 offset:36864
	v_lshl_add_u32 v42, v41, 2, v222
	ds_add_u32 v42, v224 offset:36864
	v_lshl_or_b32 v4, v16, 16, v26
	v_lshl_or_b32 v11, v40, 16, v38
	s_nop 1
	s_branch .Lidx_join
